# P7 epilogue stores: packed results permuted across the wave (ds_bpermute) so 4 consecutive lanes write 32 contiguous bytes of a row instead of 64 scattered 8-byte pieces
# speedup vs baseline: 1.0068x; 1.0068x over previous
.LBB0_866:
	s_ashr_i32 s43, s42, 31
	s_lshl_b64 s[42:43], s[42:43], 13
	v_lshl_or_b32 v18, s40, 8, v212
	s_add_u32 s42, s56, s42
	s_addc_u32 s43, s57, s43
	v_ashrrev_i32_e32 v19, 31, v18
	v_lshl_add_u64 v[2:3], v[18:19], 2, s[42:43]
	global_load_dwordx4 v[10:13], v[2:3], off
	global_load_dwordx4 v[14:17], v[2:3], off offset:16
	global_load_dwordx4 v[192:195], v[2:3], off offset:512
	global_load_dwordx4 v[196:199], v[2:3], off offset:528
	v_lshl_add_u32 v20, s80, 8, v209
	v_ashrrev_i32_e32 v21, 31, v20
	v_or_b32_e32 v4, 16, v20
	v_or_b32_e32 v6, 32, v20
	v_lshlrev_b64 v[8:9], 11, v[20:21]
	v_ashrrev_i32_e32 v5, 31, v4
	v_ashrrev_i32_e32 v7, 31, v6
	v_lshl_add_u64 v[8:9], s[16:17], 0, v[8:9]
	v_lshlrev_b64 v[30:31], 11, v[4:5]
	v_lshlrev_b64 v[6:7], 11, v[6:7]
	v_lshl_add_u64 v[4:5], v[8:9], 0, v[18:19]
	v_lshl_add_u64 v[8:9], s[16:17], 0, v[30:31]
	v_lshl_add_u64 v[30:31], s[16:17], 0, v[6:7]
	v_lshl_add_u64 v[6:7], v[8:9], 0, v[18:19]
	v_lshl_add_u64 v[8:9], v[30:31], 0, v[18:19]
	v_mov_b32_e32 v22, 0
	v_mov_b32_e32 v23, 0
	v_mov_b32_e32 v24, 0
	v_mov_b32_e32 v25, 0
	v_mov_b32_e32 v26, 0
	v_mov_b32_e32 v27, 0
	v_mov_b32_e32 v28, 0
	v_mbcnt_lo_u32_b32 v29, -1, 0
	v_mbcnt_hi_u32_b32 v29, -1, v29
	v_lshrrev_b32_e32 v202, 2, v29
	v_and_b32_e32 v203, 15, v29
	v_sub_u32_e32 v202, v202, v203
	v_and_b32_e32 v203, 3, v29
	v_bfe_u32 v250, v29, 4, 2
	v_sub_u32_e32 v203, v203, v250
	v_lshlrev_b32_e32 v202, 11, v202
	v_lshl_add_u32 v202, v203, 3, v202
	v_ashrrev_i32_e32 v203, 31, v202
	v_and_b32_e32 v250, 3, v29
	v_lshlrev_b32_e32 v250, 4, v250
	v_lshrrev_b32_e32 v29, 2, v29
	v_add_lshl_u32 v250, v250, v29, 2
	v_lshl_add_u64 v[4:5], v[4:5], 0, v[202:203]
	v_lshl_add_u64 v[6:7], v[6:7], 0, v[202:203]
	v_lshl_add_u64 v[8:9], v[8:9], 0, v[202:203]
	s_mov_b64 s[98:99], s[0:1]
	s_andn2_b64 vcc, exec, s[0:1]
	s_cbranch_vccnz .Lp7u_done
	v_mov_b32_e32 v170, v219
	v_mov_b32_e32 v166, v218
	v_mov_b32_e32 v174, v217
	v_mov_b32_e32 v172, v216
	s_mov_b32 s42, s36
	s_mov_b32 s40, s34
	s_mov_b32 s80, s79
	s_mov_b64 s[44:45], s[38:39]
	s_add_i32 s64, s64, 1
	s_mul_i32 s0, s64, s65
	s_mul_hi_u32 s1, s64, s94
	s_add_i32 s1, s1, s0
	s_mul_i32 s0, s64, s94
	v_readlane_b32 s35, v254, 18
	s_add_u32 s46, s0, s35
	s_addc_u32 s47, s1, s52
	v_cmp_ge_i64_e32 vcc, s[46:47], v[168:169]
	v_cmp_lt_i64_e64 s[0:1], s[46:47], v[168:169]
	s_cbranch_vccnz .Lp7u_861
	s_ashr_i32 s34, s46, 31
	s_lshr_b32 s34, s34, 29
	s_add_i32 s34, s46, s34
	s_ashr_i32 s35, s34, 3
	s_and_b32 s34, s34, -8
	s_sub_i32 s34, s46, s34
	s_cmp_lt_i32 s34, 0
	s_cselect_b32 s36, s50, s23
	s_mul_i32 s34, s34, s36
	s_add_i32 s34, s34, s35
	s_ashr_i32 s35, s34, 31
	s_lshr_b32 s35, s35, 26
	s_add_i32 s35, s34, s35
	s_ashr_i32 s36, s35, 6
	s_lshl_b32 s36, s36, 3
	s_sub_i32 s37, s23, s36
	s_min_i32 s37, s37, 8
	s_abs_i32 s38, s37
	v_cvt_f32_u32_e32 v32, s38
	s_sub_i32 s43, 0, s38
	s_andn2_b32 s35, s35, 63
	s_sub_i32 s35, s34, s35
	v_rcp_iflag_f32_e32 v32, v32
	s_abs_i32 s34, s35
	s_xor_b32 s39, s35, s37
	s_ashr_i32 s39, s39, 31
	v_mul_f32_e32 v32, 0x4f7ffffe, v32
	v_cvt_u32_f32_e32 v32, v32
	s_nop 0
	v_readfirstlane_b32 s46, v32
	s_mul_i32 s43, s43, s46
	s_mul_hi_u32 s43, s46, s43
	s_add_i32 s46, s46, s43
	s_mul_hi_u32 s43, s34, s46
	s_mul_i32 s46, s43, s38
	s_sub_i32 s34, s34, s46
	s_add_i32 s47, s43, 1
	s_sub_i32 s46, s34, s38
	s_cmp_ge_u32 s34, s38
	s_cselect_b32 s43, s47, s43
	s_cselect_b32 s34, s46, s34
	s_add_i32 s46, s43, 1
	s_cmp_ge_u32 s34, s38
	s_cselect_b32 s34, s46, s43
	s_xor_b32 s34, s34, s39
	s_sub_i32 s34, s34, s39
	s_mul_i32 s37, s34, s37
	s_sub_i32 s35, s35, s37
	s_add_i32 s79, s36, s35
	s_add_i32 s35, s79, 0
	s_add_i32 s35, s35, 0x22200
	v_mov_b32_e32 v32, s35
	ds_read_u8 v32, v32
	s_waitcnt lgkmcnt(0)
	v_readfirstlane_b32 s36, v32
	s_ashr_i32 s37, s36, 31
	s_lshl_b64 s[38:39], s[36:37], 22
	s_add_u32 s37, s25, s38
	s_addc_u32 s43, s33, s39
	s_ashr_i32 s35, s34, 31
	s_lshl_b64 s[38:39], s[34:35], 19
	s_add_u32 s38, s37, s38
	s_addc_u32 s39, s43, s39

.LBB0_868:
	s_nop 15
	s_nop 15
	s_waitcnt vmcnt(0)
	v_pk_mul_f32 v[30:31], v[10:11], s[22:23] op_sel_hi:[1,0]
	s_nop 0
	v_pk_fma_f32 v[32:33], v[158:159], s[24:25], v[30:31] op_sel_hi:[1,0,1]
	v_pk_mul_f32 v[12:13], v[12:13], s[22:23] op_sel_hi:[1,0]
	v_med3_f32 v21, v32, s74, v215
	v_med3_f32 v29, v33, s74, v215
	v_cvt_pk_fp8_f32 v22, v21, v29
	v_pk_mul_f32 v[14:15], v[14:15], s[22:23] op_sel_hi:[1,0]
	v_pk_fma_f32 v[10:11], v[160:161], s[24:25], v[12:13] op_sel_hi:[1,0,1]
	v_pk_fma_f32 v[130:131], v[130:131], s[24:25], v[14:15] op_sel_hi:[1,0,1]
	v_med3_f32 v10, v10, s74, v215
	v_med3_f32 v11, v11, s74, v215
	v_pk_fma_f32 v[154:155], v[154:155], s[24:25], v[14:15] op_sel_hi:[1,0,1]
	v_med3_f32 v130, v130, s74, v215
	v_cvt_pk_fp8_f32 v22, v10, v11 op_sel:[0,0,1]
	ds_bpermute_b32 v22, v250, v22
	v_med3_f32 v10, v131, s74, v215
	v_mov_b32_e32 v29, 0
	v_pk_fma_f32 v[150:151], v[150:151], s[24:25], v[30:31] op_sel_hi:[1,0,1]
	v_pk_fma_f32 v[146:147], v[146:147], s[24:25], v[14:15] op_sel_hi:[1,0,1]
	v_med3_f32 v32, v154, s74, v215
	v_med3_f32 v33, v155, s74, v215
	v_cvt_pk_fp8_f32 v29, v130, v10
	v_pk_mul_f32 v[16:17], v[16:17], s[22:23] op_sel_hi:[1,0]
	v_pk_fma_f32 v[142:143], v[142:143], s[24:25], v[30:31] op_sel_hi:[1,0,1]
	v_pk_fma_f32 v[138:139], v[138:139], s[24:25], v[14:15] op_sel_hi:[1,0,1]
	v_med3_f32 v150, v150, s74, v215
	v_med3_f32 v151, v151, s74, v215
	v_med3_f32 v146, v146, s74, v215
	v_med3_f32 v147, v147, s74, v215
	v_cvt_pk_fp8_f32 v23, v32, v33
	v_pk_fma_f32 v[132:133], v[132:133], s[24:25], v[16:17] op_sel_hi:[1,0,1]
	v_med3_f32 v142, v142, s74, v215
	v_med3_f32 v143, v143, s74, v215
	v_med3_f32 v138, v138, s74, v215
	v_med3_f32 v139, v139, s74, v215
	v_cvt_pk_fp8_f32 v24, v150, v151
	v_cvt_pk_fp8_f32 v25, v146, v147
	v_pk_fma_f32 v[156:157], v[156:157], s[24:25], v[16:17] op_sel_hi:[1,0,1]
	v_cvt_pk_fp8_f32 v26, v142, v143
	v_cvt_pk_fp8_f32 v27, v138, v139
	v_med3_f32 v10, v132, s74, v215
	v_med3_f32 v11, v133, s74, v215
	v_pk_fma_f32 v[152:153], v[152:153], s[24:25], v[12:13] op_sel_hi:[1,0,1]
	v_pk_fma_f32 v[148:149], v[148:149], s[24:25], v[16:17] op_sel_hi:[1,0,1]
	v_med3_f32 v154, v156, s74, v215
	v_med3_f32 v155, v157, s74, v215
	v_cvt_pk_fp8_f32 v29, v10, v11 op_sel:[0,0,1]
	ds_bpermute_b32 v29, v250, v29
	v_or_b32_e32 v10, 48, v20
	v_pk_fma_f32 v[144:145], v[144:145], s[24:25], v[12:13] op_sel_hi:[1,0,1]
	v_pk_fma_f32 v[140:141], v[140:141], s[24:25], v[16:17] op_sel_hi:[1,0,1]
	v_med3_f32 v152, v152, s74, v215
	v_med3_f32 v153, v153, s74, v215
	v_med3_f32 v148, v148, s74, v215
	v_med3_f32 v149, v149, s74, v215
	v_cvt_pk_fp8_f32 v23, v154, v155 op_sel:[0,0,1]
	ds_bpermute_b32 v23, v250, v23
	v_ashrrev_i32_e32 v11, 31, v10
	v_med3_f32 v144, v144, s74, v215
	v_med3_f32 v145, v145, s74, v215
	v_med3_f32 v140, v140, s74, v215
	v_med3_f32 v141, v141, s74, v215
	v_cvt_pk_fp8_f32 v24, v152, v153 op_sel:[0,0,1]
	ds_bpermute_b32 v24, v250, v24
	v_cvt_pk_fp8_f32 v25, v148, v149 op_sel:[0,0,1]
	ds_bpermute_b32 v25, v250, v25
	v_lshlrev_b64 v[10:11], 11, v[10:11]
	v_cvt_pk_fp8_f32 v26, v144, v145 op_sel:[0,0,1]
	ds_bpermute_b32 v26, v250, v26
	v_cvt_pk_fp8_f32 v27, v140, v141 op_sel:[0,0,1]
	ds_bpermute_b32 v27, v250, v27
	v_lshl_add_u64 v[10:11], s[16:17], 0, v[10:11]
	v_lshl_add_u64 v[10:11], v[10:11], 0, v[18:19]
	v_lshl_add_u64 v[10:11], v[10:11], 0, v[202:203]
	v_pk_fma_f32 v[18:19], v[128:129], s[24:25], v[12:13] op_sel_hi:[1,0,1]
	v_pk_fma_f32 v[20:21], v[126:127], s[24:25], v[30:31] op_sel_hi:[1,0,1]
	s_waitcnt lgkmcnt(0)
	global_store_dwordx2 v[4:5], v[22:23], off
	global_store_dwordx2 v[6:7], v[24:25], off
	global_store_dwordx2 v[8:9], v[26:27], off
	v_pk_fma_f32 v[24:25], v[122:123], s[24:25], v[14:15] op_sel_hi:[1,0,1]
	v_med3_f32 v20, v20, s74, v215
	v_med3_f32 v21, v21, s74, v215
	v_med3_f32 v26, v18, s74, v215
	v_mov_b32_e32 v18, 0
	v_med3_f32 v27, v19, s74, v215
	v_cvt_pk_fp8_f32 v18, v20, v21
	v_med3_f32 v20, v24, s74, v215
	v_med3_f32 v21, v25, s74, v215
	v_mov_b32_e32 v19, 0
	v_cvt_pk_fp8_f32 v19, v20, v21
	v_pk_fma_f32 v[22:23], v[124:125], s[24:25], v[16:17] op_sel_hi:[1,0,1]
	v_cvt_pk_fp8_f32 v18, v26, v27 op_sel:[0,0,1]
	ds_bpermute_b32 v18, v250, v18
	v_med3_f32 v20, v22, s74, v215
	v_med3_f32 v21, v23, s74, v215
	v_cvt_pk_fp8_f32 v19, v20, v21 op_sel:[0,0,1]
	ds_bpermute_b32 v19, v250, v19
	v_add_co_u32_e32 v20, vcc, s75, v4
	v_pk_fma_f32 v[24:25], v[114:115], s[24:25], v[14:15] op_sel_hi:[1,0,1]
	s_nop 0
	v_addc_co_u32_e32 v21, vcc, 0, v5, vcc
	s_waitcnt lgkmcnt(0)
	global_store_dwordx2 v[20:21], v[18:19], off
	v_pk_fma_f32 v[18:19], v[120:121], s[24:25], v[12:13] op_sel_hi:[1,0,1]
	v_pk_fma_f32 v[20:21], v[118:119], s[24:25], v[30:31] op_sel_hi:[1,0,1]
	v_med3_f32 v26, v18, s74, v215
	v_med3_f32 v20, v20, s74, v215
	v_med3_f32 v21, v21, s74, v215
	v_mov_b32_e32 v18, 0
	v_med3_f32 v27, v19, s74, v215
	v_cvt_pk_fp8_f32 v18, v20, v21
	v_med3_f32 v20, v24, s74, v215
	v_med3_f32 v21, v25, s74, v215
	v_mov_b32_e32 v19, 0
	v_cvt_pk_fp8_f32 v19, v20, v21
	v_pk_fma_f32 v[22:23], v[116:117], s[24:25], v[16:17] op_sel_hi:[1,0,1]
	v_cvt_pk_fp8_f32 v18, v26, v27 op_sel:[0,0,1]
	ds_bpermute_b32 v18, v250, v18
	v_med3_f32 v20, v22, s74, v215
	v_med3_f32 v21, v23, s74, v215
	v_cvt_pk_fp8_f32 v19, v20, v21 op_sel:[0,0,1]
	ds_bpermute_b32 v19, v250, v19
	v_add_co_u32_e32 v20, vcc, s76, v4
	v_pk_fma_f32 v[24:25], v[106:107], s[24:25], v[14:15] op_sel_hi:[1,0,1]
	s_nop 0
	v_addc_co_u32_e32 v21, vcc, 0, v5, vcc
	s_waitcnt lgkmcnt(0)
	global_store_dwordx2 v[20:21], v[18:19], off
	v_pk_fma_f32 v[18:19], v[112:113], s[24:25], v[12:13] op_sel_hi:[1,0,1]
	v_pk_fma_f32 v[20:21], v[110:111], s[24:25], v[30:31] op_sel_hi:[1,0,1]
	v_med3_f32 v26, v18, s74, v215
	v_med3_f32 v20, v20, s74, v215
	v_med3_f32 v21, v21, s74, v215
	v_mov_b32_e32 v18, 0
	v_med3_f32 v27, v19, s74, v215
	v_cvt_pk_fp8_f32 v18, v20, v21
	v_med3_f32 v20, v24, s74, v215
	v_med3_f32 v21, v25, s74, v215
	v_mov_b32_e32 v19, 0
	v_cvt_pk_fp8_f32 v19, v20, v21
	v_pk_fma_f32 v[22:23], v[108:109], s[24:25], v[16:17] op_sel_hi:[1,0,1]
	v_cvt_pk_fp8_f32 v18, v26, v27 op_sel:[0,0,1]
	ds_bpermute_b32 v18, v250, v18
	v_med3_f32 v20, v22, s74, v215
	v_med3_f32 v21, v23, s74, v215
	v_cvt_pk_fp8_f32 v19, v20, v21 op_sel:[0,0,1]
	ds_bpermute_b32 v19, v250, v19
	v_add_co_u32_e32 v20, vcc, s77, v4
	v_pk_fma_f32 v[136:137], v[136:137], s[24:25], v[12:13] op_sel_hi:[1,0,1]
	s_nop 0
	v_addc_co_u32_e32 v21, vcc, 0, v5, vcc
	v_pk_fma_f32 v[134:135], v[134:135], s[24:25], v[30:31] op_sel_hi:[1,0,1]
	s_waitcnt lgkmcnt(0)
	global_store_dwordx2 v[20:21], v[18:19], off
	v_pk_fma_f32 v[12:13], v[100:101], s[24:25], v[12:13] op_sel_hi:[1,0,1]
	v_pk_fma_f32 v[18:19], v[98:99], s[24:25], v[30:31] op_sel_hi:[1,0,1]
	v_pk_fma_f32 v[14:15], v[90:91], s[24:25], v[14:15] op_sel_hi:[1,0,1]
	v_med3_f32 v134, v134, s74, v215
	v_med3_f32 v135, v135, s74, v215
	v_med3_f32 v18, v18, s74, v215
	v_med3_f32 v19, v19, s74, v215
	v_med3_f32 v20, v12, s74, v215
	v_med3_f32 v21, v13, s74, v215
	v_mov_b32_e32 v12, 0
	v_med3_f32 v14, v14, s74, v215
	v_med3_f32 v15, v15, s74, v215
	v_mov_b32_e32 v13, 0
	v_cvt_pk_fp8_f32 v28, v134, v135
	v_cvt_pk_fp8_f32 v12, v18, v19
	v_cvt_pk_fp8_f32 v13, v14, v15
	v_pk_fma_f32 v[16:17], v[92:93], s[24:25], v[16:17] op_sel_hi:[1,0,1]
	v_med3_f32 v136, v136, s74, v215
	v_med3_f32 v137, v137, s74, v215
	v_med3_f32 v14, v16, s74, v215
	v_med3_f32 v15, v17, s74, v215
	v_cvt_pk_fp8_f32 v28, v136, v137 op_sel:[0,0,1]
	ds_bpermute_b32 v28, v250, v28
	v_cvt_pk_fp8_f32 v12, v20, v21 op_sel:[0,0,1]
	ds_bpermute_b32 v12, v250, v12
	v_cvt_pk_fp8_f32 v13, v14, v15 op_sel:[0,0,1]
	ds_bpermute_b32 v13, v250, v13
	v_add_co_u32_e32 v14, vcc, s78, v4
	s_waitcnt lgkmcnt(0)
	global_store_dwordx2 v[10:11], v[28:29], off
	s_nop 0
	v_addc_co_u32_e32 v15, vcc, 0, v5, vcc
	s_waitcnt lgkmcnt(0)
	global_store_dwordx2 v[14:15], v[12:13], off
	v_lshl_add_u64 v[2:3], v[4:5], 0, s[12:13]
	v_lshl_add_u64 v[20:21], v[4:5], 0, s[26:27]
	v_lshl_add_u64 v[22:23], v[4:5], 0, s[28:29]
	v_lshl_add_u64 v[24:25], v[4:5], 0, s[30:31]
	s_andn2_b64 vcc, exec, s[98:99]
	v_pk_mul_f32 v[14:15], v[194:195], s[22:23] op_sel_hi:[1,0]
	v_pk_mul_f32 v[12:13], v[192:193], s[22:23] op_sel_hi:[1,0]
	v_pk_mul_f32 v[16:17], v[196:197], s[22:23] op_sel_hi:[1,0]
	v_pk_fma_f32 v[26:27], v[104:105], s[24:25], v[14:15] op_sel_hi:[1,0,1]
	v_pk_fma_f32 v[28:29], v[102:103], s[24:25], v[12:13] op_sel_hi:[1,0,1]
	v_pk_fma_f32 v[32:33], v[94:95], s[24:25], v[16:17] op_sel_hi:[1,0,1]
	v_med3_f32 v28, v28, s74, v215
	v_med3_f32 v29, v29, s74, v215
	v_med3_f32 v90, v26, s74, v215
	v_mov_b32_e32 v26, 0
	v_med3_f32 v91, v27, s74, v215
	v_cvt_pk_fp8_f32 v26, v28, v29
	v_med3_f32 v28, v32, s74, v215
	v_med3_f32 v29, v33, s74, v215
	v_mov_b32_e32 v27, 0
	v_cvt_pk_fp8_f32 v27, v28, v29
	v_pk_mul_f32 v[18:19], v[198:199], s[22:23] op_sel_hi:[1,0]
	v_pk_fma_f32 v[82:83], v[82:83], s[24:25], v[16:17] op_sel_hi:[1,0,1]
	v_pk_fma_f32 v[30:31], v[96:97], s[24:25], v[18:19] op_sel_hi:[1,0,1]
	v_pk_fma_f32 v[32:33], v[84:85], s[24:25], v[18:19] op_sel_hi:[1,0,1]
	v_med3_f32 v28, v30, s74, v215
	v_med3_f32 v29, v31, s74, v215
	v_cvt_pk_fp8_f32 v27, v28, v29 op_sel:[0,0,1]
	ds_bpermute_b32 v27, v250, v27
	v_pk_fma_f32 v[28:29], v[88:89], s[24:25], v[14:15] op_sel_hi:[1,0,1]
	v_pk_fma_f32 v[30:31], v[86:87], s[24:25], v[12:13] op_sel_hi:[1,0,1]
	v_med3_f32 v84, v28, s74, v215
	v_med3_f32 v30, v30, s74, v215
	v_med3_f32 v31, v31, s74, v215
	v_mov_b32_e32 v28, 0
	v_med3_f32 v85, v29, s74, v215
	v_cvt_pk_fp8_f32 v28, v30, v31
	v_med3_f32 v30, v82, s74, v215
	v_med3_f32 v31, v83, s74, v215
	v_mov_b32_e32 v29, 0
	v_cvt_pk_fp8_f32 v29, v30, v31
	v_med3_f32 v30, v32, s74, v215
	v_med3_f32 v31, v33, s74, v215
	v_pk_fma_f32 v[32:33], v[78:79], s[24:25], v[12:13] op_sel_hi:[1,0,1]
	v_cvt_pk_fp8_f32 v29, v30, v31 op_sel:[0,0,1]
	ds_bpermute_b32 v29, v250, v29
	v_pk_fma_f32 v[30:31], v[80:81], s[24:25], v[14:15] op_sel_hi:[1,0,1]
	v_pk_fma_f32 v[74:75], v[74:75], s[24:25], v[16:17] op_sel_hi:[1,0,1]
	v_med3_f32 v32, v32, s74, v215
	v_med3_f32 v33, v33, s74, v215
	v_med3_f32 v78, v30, s74, v215
	v_mov_b32_e32 v30, 0
	v_med3_f32 v79, v31, s74, v215
	v_cvt_pk_fp8_f32 v30, v32, v33
	v_med3_f32 v32, v74, s74, v215
	v_med3_f32 v33, v75, s74, v215
	v_mov_b32_e32 v31, 0
	v_cvt_pk_fp8_f32 v31, v32, v33
	v_pk_fma_f32 v[76:77], v[76:77], s[24:25], v[18:19] op_sel_hi:[1,0,1]
	v_pk_fma_f32 v[70:71], v[70:71], s[24:25], v[12:13] op_sel_hi:[1,0,1]
	v_med3_f32 v32, v76, s74, v215
	v_med3_f32 v33, v77, s74, v215
	v_cvt_pk_fp8_f32 v31, v32, v33 op_sel:[0,0,1]
	ds_bpermute_b32 v31, v250, v31
	v_pk_fma_f32 v[32:33], v[72:73], s[24:25], v[14:15] op_sel_hi:[1,0,1]
	v_pk_fma_f32 v[66:67], v[66:67], s[24:25], v[16:17] op_sel_hi:[1,0,1]
	v_med3_f32 v70, v70, s74, v215
	v_med3_f32 v71, v71, s74, v215
	v_med3_f32 v72, v32, s74, v215
	v_med3_f32 v73, v33, s74, v215
	v_mov_b32_e32 v32, 0
	v_med3_f32 v66, v66, s74, v215
	v_med3_f32 v67, v67, s74, v215
	v_mov_b32_e32 v33, 0
	v_cvt_pk_fp8_f32 v32, v70, v71
	v_cvt_pk_fp8_f32 v33, v66, v67
	v_cvt_pk_fp8_f32 v26, v90, v91 op_sel:[0,0,1]
	ds_bpermute_b32 v26, v250, v26
	v_cvt_pk_fp8_f32 v28, v84, v85 op_sel:[0,0,1]
	ds_bpermute_b32 v28, v250, v28
	v_pk_fma_f32 v[68:69], v[68:69], s[24:25], v[18:19] op_sel_hi:[1,0,1]
	v_cvt_pk_fp8_f32 v30, v78, v79 op_sel:[0,0,1]
	ds_bpermute_b32 v30, v250, v30
	v_med3_f32 v66, v68, s74, v215
	v_med3_f32 v67, v69, s74, v215
	v_cvt_pk_fp8_f32 v32, v72, v73 op_sel:[0,0,1]
	ds_bpermute_b32 v32, v250, v32
	v_cvt_pk_fp8_f32 v33, v66, v67 op_sel:[0,0,1]
	ds_bpermute_b32 v33, v250, v33
	s_waitcnt lgkmcnt(0)
	global_store_dwordx2 v[4:5], v[26:27], off offset:128
	global_store_dwordx2 v[6:7], v[28:29], off offset:128
	global_store_dwordx2 v[8:9], v[30:31], off offset:128
	global_store_dwordx2 v[10:11], v[32:33], off offset:128
	v_pk_fma_f32 v[4:5], v[64:65], s[24:25], v[14:15] op_sel_hi:[1,0,1]
	v_pk_fma_f32 v[6:7], v[62:63], s[24:25], v[12:13] op_sel_hi:[1,0,1]
	v_pk_fma_f32 v[10:11], v[58:59], s[24:25], v[16:17] op_sel_hi:[1,0,1]
	v_med3_f32 v6, v6, s74, v215
	v_med3_f32 v7, v7, s74, v215
	v_med3_f32 v26, v4, s74, v215
	v_mov_b32_e32 v4, 0
	v_med3_f32 v27, v5, s74, v215
	v_cvt_pk_fp8_f32 v4, v6, v7
	v_med3_f32 v6, v10, s74, v215
	v_med3_f32 v7, v11, s74, v215
	v_mov_b32_e32 v5, 0
	v_cvt_pk_fp8_f32 v5, v6, v7
	v_pk_fma_f32 v[8:9], v[60:61], s[24:25], v[18:19] op_sel_hi:[1,0,1]
	v_cvt_pk_fp8_f32 v4, v26, v27 op_sel:[0,0,1]
	ds_bpermute_b32 v4, v250, v4
	v_med3_f32 v6, v8, s74, v215
	v_med3_f32 v7, v9, s74, v215
	v_cvt_pk_fp8_f32 v5, v6, v7 op_sel:[0,0,1]
	ds_bpermute_b32 v5, v250, v5
	v_pk_fma_f32 v[6:7], v[56:57], s[24:25], v[14:15] op_sel_hi:[1,0,1]
	v_pk_fma_f32 v[8:9], v[54:55], s[24:25], v[12:13] op_sel_hi:[1,0,1]
	v_pk_fma_f32 v[26:27], v[50:51], s[24:25], v[16:17] op_sel_hi:[1,0,1]
	v_med3_f32 v8, v8, s74, v215
	v_med3_f32 v9, v9, s74, v215
	v_med3_f32 v28, v6, s74, v215
	v_mov_b32_e32 v6, 0
	v_med3_f32 v29, v7, s74, v215
	v_cvt_pk_fp8_f32 v6, v8, v9
	v_med3_f32 v8, v26, s74, v215
	v_med3_f32 v9, v27, s74, v215
	v_mov_b32_e32 v7, 0
	v_cvt_pk_fp8_f32 v7, v8, v9
	v_pk_fma_f32 v[10:11], v[52:53], s[24:25], v[18:19] op_sel_hi:[1,0,1]
	v_cvt_pk_fp8_f32 v6, v28, v29 op_sel:[0,0,1]
	ds_bpermute_b32 v6, v250, v6
	v_med3_f32 v8, v10, s74, v215
	v_med3_f32 v9, v11, s74, v215
	v_cvt_pk_fp8_f32 v7, v8, v9 op_sel:[0,0,1]
	ds_bpermute_b32 v7, v250, v7
	v_pk_fma_f32 v[8:9], v[48:49], s[24:25], v[14:15] op_sel_hi:[1,0,1]
	v_pk_fma_f32 v[10:11], v[46:47], s[24:25], v[12:13] op_sel_hi:[1,0,1]
	v_pk_fma_f32 v[28:29], v[42:43], s[24:25], v[16:17] op_sel_hi:[1,0,1]
	v_med3_f32 v10, v10, s74, v215
	v_med3_f32 v11, v11, s74, v215
	v_med3_f32 v30, v8, s74, v215
	v_mov_b32_e32 v8, 0
	v_med3_f32 v31, v9, s74, v215
	v_cvt_pk_fp8_f32 v8, v10, v11
	v_med3_f32 v10, v28, s74, v215
	v_med3_f32 v11, v29, s74, v215
	v_mov_b32_e32 v9, 0
	v_cvt_pk_fp8_f32 v9, v10, v11
	v_pk_fma_f32 v[26:27], v[44:45], s[24:25], v[18:19] op_sel_hi:[1,0,1]
	v_pk_fma_f32 v[12:13], v[38:39], s[24:25], v[12:13] op_sel_hi:[1,0,1]
	v_med3_f32 v10, v26, s74, v215
	v_med3_f32 v11, v27, s74, v215
	v_cvt_pk_fp8_f32 v9, v10, v11 op_sel:[0,0,1]
	ds_bpermute_b32 v9, v250, v9
	v_pk_fma_f32 v[10:11], v[40:41], s[24:25], v[14:15] op_sel_hi:[1,0,1]
	v_pk_fma_f32 v[14:15], v[36:37], s[24:25], v[18:19] op_sel_hi:[1,0,1]
	v_pk_fma_f32 v[16:17], v[34:35], s[24:25], v[16:17] op_sel_hi:[1,0,1]
	v_med3_f32 v12, v12, s74, v215
	v_med3_f32 v13, v13, s74, v215
	v_med3_f32 v18, v10, s74, v215
	v_mov_b32_e32 v10, 0
	v_med3_f32 v19, v11, s74, v215
	v_cvt_pk_fp8_f32 v10, v12, v13
	v_med3_f32 v12, v16, s74, v215
	v_med3_f32 v13, v17, s74, v215
	v_mov_b32_e32 v11, 0
	v_cvt_pk_fp8_f32 v11, v12, v13
	v_cvt_pk_fp8_f32 v8, v30, v31 op_sel:[0,0,1]
	ds_bpermute_b32 v8, v250, v8
	v_med3_f32 v12, v14, s74, v215
	v_med3_f32 v13, v15, s74, v215
	v_cvt_pk_fp8_f32 v10, v18, v19 op_sel:[0,0,1]
	ds_bpermute_b32 v10, v250, v10
	v_cvt_pk_fp8_f32 v11, v12, v13 op_sel:[0,0,1]
	ds_bpermute_b32 v11, v250, v11
	s_waitcnt lgkmcnt(0)
	global_store_dwordx2 v[2:3], v[4:5], off offset:128
	global_store_dwordx2 v[20:21], v[6:7], off offset:128
	global_store_dwordx2 v[22:23], v[8:9], off offset:128
	global_store_dwordx2 v[24:25], v[10:11], off offset:128
	s_cbranch_vccnz .LBB0_871
	s_branch .Lp7_entry_pre
